# conversion store step back to one LDS read and one store at a time (original form), everything else as the packed-SwiGLU version
# speedup vs baseline: 1.0042x; 1.0042x over previous
; #define GAS __attribute__((address_space(1)))
; #define LAS __attribute__((address_space(3)))
; __device__ __forceinline__ void cv8_out(const CvTile& cur, const LAS unsigned char* T, int tid_) {
;     const int nbl = cur.N / 256, kb = cur.r / nbl, nb = cur.r - kb * nbl;
; #pragma unroll
;     for (int i = 0; i < 4; ++i) { const int p = tid_ + 512 * i, c = p & 7, n = p >> 3, nn = 256 * nb + n;
;         const int drow = (cur.mode == 0) ? nn : (256 * (nn >> 7) + (nn & 127) + (cur.mode == 2 ? 128 : 0));
;         const v4u w = *(const LAS v4u*)(T + n * 128 + 16 * (c ^ ((n >> 2) & 7)));
;         __builtin_nontemporal_store(w, (GAS v4u*)(cur.WT + (size_t)drow * cur.K + 128 * kb + 16 * c)); }
; }
.LBB0_494:
	s_waitcnt vmcnt(15)
	v_add_u32_e32 v2, s64, v102
	v_lshlrev_b32_e32 v3, 1, v2
	v_and_b32_e32 v3, 0xffffff00, v3
	v_or3_b32 v3, v100, v3, s18
	s_waitcnt vmcnt(13)
	v_add_u32_e32 v10, s22, v101
	v_cndmask_b32_e64 v8, v3, v2, s[62:63]
	v_add_u32_e32 v2, v10, v99
	v_ashrrev_i32_e32 v6, 31, v8
	ds_read_b128 v[2:5], v2
	v_mul_lo_u32 v11, s60, v6
	v_mov_b64_e32 v[6:7], s[58:59]
	v_mul_lo_u32 v12, s61, v8
	v_mad_u64_u32 v[8:9], s[0:1], s60, v8, v[6:7]
	s_ashr_i32 s71, s70, 31
	v_add3_u32 v9, v12, v9, v11
	v_lshl_add_u64 v[8:9], v[8:9], 0, s[70:71]
	v_lshl_add_u64 v[8:9], v[8:9], 0, v[0:1]
	s_waitcnt lgkmcnt(0)
	global_store_dwordx4 v[8:9], v[2:5], off nt
	s_nop 1
	v_add_u32_e32 v2, s64, v98
	v_lshlrev_b32_e32 v3, 1, v2
	v_and_b32_e32 v3, 0xffffff00, v3
	v_or3_b32 v3, v97, v3, s18
	v_cndmask_b32_e64 v8, v3, v2, s[62:63]
	v_add_u32_e32 v2, v10, v96
	ds_read_b128 v[2:5], v2
	v_ashrrev_i32_e32 v9, 31, v8
	v_mul_lo_u32 v11, s60, v9
	v_mul_lo_u32 v12, s61, v8
	v_mad_u64_u32 v[8:9], s[0:1], s60, v8, v[6:7]
	v_add3_u32 v9, v12, v9, v11
	v_lshl_add_u64 v[8:9], v[8:9], 0, s[70:71]
	v_lshl_add_u64 v[8:9], v[8:9], 0, v[0:1]
	s_waitcnt lgkmcnt(0)
	global_store_dwordx4 v[8:9], v[2:5], off nt
	s_nop 1
	v_add_u32_e32 v2, s64, v94
	v_lshlrev_b32_e32 v3, 1, v2
	v_and_b32_e32 v3, 0xffffff00, v3
	v_or3_b32 v3, v93, v3, s18
	v_cndmask_b32_e64 v8, v3, v2, s[62:63]
	v_add_u32_e32 v2, v10, v92
	ds_read_b128 v[2:5], v2
	v_ashrrev_i32_e32 v9, 31, v8
	v_mul_lo_u32 v11, s60, v9
	v_mul_lo_u32 v12, s61, v8
	v_mad_u64_u32 v[8:9], s[0:1], s60, v8, v[6:7]
	v_add3_u32 v9, v12, v9, v11
	v_lshl_add_u64 v[8:9], v[8:9], 0, s[70:71]
	v_lshl_add_u64 v[8:9], v[8:9], 0, v[0:1]
	s_waitcnt lgkmcnt(0)
	global_store_dwordx4 v[8:9], v[2:5], off nt
	s_nop 1
	v_add_u32_e32 v2, s64, v91
	v_lshlrev_b32_e32 v3, 1, v2
	v_and_b32_e32 v3, 0xffffff00, v3
	v_or3_b32 v3, v90, v3, s18
	v_cndmask_b32_e64 v8, v3, v2, s[62:63]
	v_add_u32_e32 v2, v10, v89
	ds_read_b128 v[2:5], v2
	v_ashrrev_i32_e32 v9, 31, v8
	v_mul_lo_u32 v9, s60, v9
	v_mul_lo_u32 v10, s61, v8
	v_mad_u64_u32 v[6:7], s[0:1], s60, v8, v[6:7]
	v_add3_u32 v7, v10, v7, v9
	v_lshl_add_u64 v[6:7], v[6:7], 0, s[70:71]
	v_lshl_add_u64 v[6:7], v[6:7], 0, v[0:1]
	s_waitcnt lgkmcnt(0)
	global_store_dwordx4 v[6:7], v[2:5], off nt
	s_waitcnt lgkmcnt(0)
	s_branch .LBB0_499
